# attention QK^T tiles: LDS fragment reads software-pipelined 2-3 MFMAs ahead (rotating register sets)
# baseline (speedup 1.0000x reference)
; #define LAS __attribute__((address_space(3)))
; #define SBAR() __builtin_amdgcn_sched_barrier(0)
; template <int KB>
; __device__ __forceinline__ void qkt(f32x16& p0, f32x16& p1, LAS const unsigned char* K_lds, LAS const unsigned char* q_lds, int r32, int hi) {
;     p0 = f32x16{}; p1 = f32x16{};
;     LAS const unsigned char* kb[4];
; #pragma unroll
;     for (int dd = 0; dd < 4; ++dd) kb[dd] = K_lds + KB * SHM_K + KSWZ(r32, (dd * 16 + hi * 8) * 2);
; #pragma unroll
;     for (int d0 = 0; d0 < 8; ++d0) { LAS const unsigned char* a = kb[d0 & 3] + (d0 >> 2) * 128;
;         const bf16x8 b0 = *(LAS const bf16x8*)(a);
;         const bf16x8 b1 = *(LAS const bf16x8*)(a + 32 * 256);
;         const bf16x8 qv = *(LAS const bf16x8*)(q_lds + d0 * 1024);
;         p0 = __builtin_amdgcn_mfma_f32_32x32x16_bf16(b0, qv, p0, 0, 0, 0);
;         p1 = __builtin_amdgcn_mfma_f32_32x32x16_bf16(b1, qv, p1, 0, 0, 0);
;         if ((d0 & 3) == 3) SBAR(); }
; }
.LBB0_627:
	v_add_u32_e32 v0, v206, v207
	ds_read_b128 v[66:69], v0 offset:32768
	ds_read_b128 v[70:73], v204
	v_add_u32_e32 v213, v206, v208
	ds_read_b128 v[214:217], v0 offset:40960
	ds_read_b128 v[138:141], v213 offset:32768
	ds_read_b128 v[218:221], v204 offset:1024
	v_add_u32_e32 v222, v206, v209
	v_add_u32_e32 v223, v206, v210
	ds_read_b128 v[246:249], v213 offset:40960
	ds_read_b128 v[250:253], v204 offset:2048
	s_waitcnt lgkmcnt(5)
	v_mfma_f32_32x32x16_bf16 v[82:97], v[66:69], v[70:73], 0
	s_waitcnt lgkmcnt(4)
	v_mfma_f32_32x32x16_bf16 v[66:81], v[214:217], v[70:73], 0
	ds_read_b128 v[214:217], v222 offset:32768
	s_waitcnt lgkmcnt(3)
	v_mfma_f32_32x32x16_bf16 v[82:97], v[138:141], v[218:221], v[82:97]
	ds_read_b128 v[138:141], v222 offset:40960
	s_waitcnt lgkmcnt(3)
	v_mfma_f32_32x32x16_bf16 v[66:81], v[246:249], v[218:221], v[66:81]
	ds_read_b128 v[246:249], v223 offset:32768
	ds_read_b128 v[218:221], v204 offset:3072
	s_waitcnt lgkmcnt(3)
	v_mfma_f32_32x32x16_bf16 v[82:97], v[214:217], v[250:253], v[82:97]
	ds_read_b128 v[214:217], v223 offset:40960
	s_waitcnt lgkmcnt(3)
	v_mfma_f32_32x32x16_bf16 v[66:81], v[138:141], v[250:253], v[66:81]
	ds_read_b128 v[138:141], v0 offset:32896
	ds_read_b128 v[250:253], v204 offset:4096
	s_waitcnt lgkmcnt(3)
	v_mfma_f32_32x32x16_bf16 v[82:97], v[246:249], v[218:221], v[82:97]
	ds_read_b128 v[246:249], v0 offset:41088
	s_waitcnt lgkmcnt(3)
	v_mfma_f32_32x32x16_bf16 v[66:81], v[214:217], v[218:221], v[66:81]
	ds_read_b128 v[214:217], v213 offset:32896
	ds_read_b128 v[218:221], v204 offset:5120
	s_waitcnt lgkmcnt(3)
	v_mfma_f32_32x32x16_bf16 v[82:97], v[138:141], v[250:253], v[82:97]
	ds_read_b128 v[138:141], v213 offset:41088
	s_waitcnt lgkmcnt(3)
	v_mfma_f32_32x32x16_bf16 v[66:81], v[246:249], v[250:253], v[66:81]
	ds_read_b128 v[246:249], v222 offset:32896
	ds_read_b128 v[250:253], v204 offset:6144
	s_waitcnt lgkmcnt(3)
	v_mfma_f32_32x32x16_bf16 v[82:97], v[214:217], v[218:221], v[82:97]
	ds_read_b128 v[214:217], v222 offset:41088
	s_waitcnt lgkmcnt(3)
	v_mfma_f32_32x32x16_bf16 v[66:81], v[138:141], v[218:221], v[66:81]
	ds_read_b128 v[138:141], v223 offset:32896
	ds_read_b128 v[218:221], v204 offset:7168
	s_waitcnt lgkmcnt(3)
	v_mfma_f32_32x32x16_bf16 v[82:97], v[246:249], v[250:253], v[82:97]
	ds_read_b128 v[246:249], v223 offset:41088
	s_waitcnt lgkmcnt(3)
	v_mfma_f32_32x32x16_bf16 v[66:81], v[214:217], v[250:253], v[66:81]
	s_waitcnt lgkmcnt(1)
	v_mfma_f32_32x32x16_bf16 v[82:97], v[138:141], v[218:221], v[82:97]
	s_waitcnt lgkmcnt(0)
	v_mfma_f32_32x32x16_bf16 v[66:81], v[246:249], v[218:221], v[66:81]
	s_mov_b64 s[12:13], -1
	s_and_b64 vcc, exec, s[14:15]
	s_cbranch_vccz .LBB0_631
	s_nop 5
	v_mov_b32_e32 v213, v97
	v_mov_b32_e32 v214, v96
	v_mov_b32_e32 v215, v95
	v_mov_b32_e32 v216, v94
	v_mov_b32_e32 v217, v93
	v_mov_b32_e32 v218, v92
	v_mov_b32_e32 v219, v91
	v_mov_b32_e32 v220, v90
	v_mov_b32_e32 v221, v89
	v_mov_b32_e32 v223, v88
	v_mov_b32_e32 v225, v87
	v_mov_b32_e32 v226, v86
	v_mov_b32_e32 v229, v85
	v_mov_b32_e32 v230, v84
	v_mov_b32_e32 v0, v83
	v_mov_b32_e32 v233, v82
	v_mov_b32_e32 v222, v81
	v_mov_b32_e32 v224, v80
	v_mov_b32_e32 v227, v79
	v_mov_b32_e32 v228, v78
	v_mov_b32_e32 v231, v77
	v_mov_b32_e32 v232, v76
	v_mov_b32_e32 v234, v75
	v_mov_b32_e32 v235, v74
	v_mov_b32_e32 v237, v73
	v_mov_b32_e32 v238, v72
	v_mov_b32_e32 v239, v71
	v_mov_b32_e32 v240, v70
	v_mov_b32_e32 v241, v69
	v_mov_b32_e32 v242, v68
	v_mov_b32_e32 v243, v67
	v_mov_b32_e32 v244, v66
	s_and_saveexec_b64 s[12:13], s[10:11]
	s_cbranch_execz .LBB0_630
	v_mov_b32_e32 v213, 0xff800000
	v_mov_b32_e32 v214, 0xff800000
	v_mov_b32_e32 v215, 0xff800000
	v_mov_b32_e32 v216, 0xff800000
	v_mov_b32_e32 v217, 0xff800000
	v_mov_b32_e32 v218, 0xff800000
	v_mov_b32_e32 v219, 0xff800000
	v_mov_b32_e32 v220, 0xff800000
	v_mov_b32_e32 v221, 0xff800000
	v_mov_b32_e32 v223, 0xff800000
	v_mov_b32_e32 v225, 0xff800000
	v_mov_b32_e32 v226, 0xff800000
	v_mov_b32_e32 v229, 0xff800000
	v_mov_b32_e32 v230, 0xff800000
	v_mov_b32_e32 v0, 0xff800000
	v_mov_b32_e32 v233, 0xff800000
	v_mov_b32_e32 v222, 0xff800000
	v_mov_b32_e32 v224, 0xff800000
	v_mov_b32_e32 v227, 0xff800000
	v_mov_b32_e32 v228, 0xff800000
	v_mov_b32_e32 v231, 0xff800000
	v_mov_b32_e32 v232, 0xff800000
	v_mov_b32_e32 v234, 0xff800000
	v_mov_b32_e32 v235, 0xff800000
	v_mov_b32_e32 v237, 0xff800000
	v_mov_b32_e32 v238, 0xff800000
	v_mov_b32_e32 v239, 0xff800000
	v_mov_b32_e32 v240, 0xff800000
	v_mov_b32_e32 v241, 0xff800000
	v_mov_b32_e32 v242, 0xff800000
	v_mov_b32_e32 v243, 0xff800000
	v_mov_b32_e32 v244, 0xff800000

; #define LAS __attribute__((address_space(3)))
; #define SBAR() __builtin_amdgcn_sched_barrier(0)
; template <int KB>
; __device__ __forceinline__ void qkt(f32x16& p0, f32x16& p1, LAS const unsigned char* K_lds, LAS const unsigned char* q_lds, int r32, int hi) {
;     p0 = f32x16{}; p1 = f32x16{};
;     LAS const unsigned char* kb[4];
; #pragma unroll
;     for (int dd = 0; dd < 4; ++dd) kb[dd] = K_lds + KB * SHM_K + KSWZ(r32, (dd * 16 + hi * 8) * 2);
; #pragma unroll
;     for (int d0 = 0; d0 < 8; ++d0) { LAS const unsigned char* a = kb[d0 & 3] + (d0 >> 2) * 128;
;         const bf16x8 b0 = *(LAS const bf16x8*)(a);
;         const bf16x8 b1 = *(LAS const bf16x8*)(a + 32 * 256);
;         const bf16x8 qv = *(LAS const bf16x8*)(q_lds + d0 * 1024);
;         p0 = __builtin_amdgcn_mfma_f32_32x32x16_bf16(b0, qv, p0, 0, 0, 0);
;         p1 = __builtin_amdgcn_mfma_f32_32x32x16_bf16(b1, qv, p1, 0, 0, 0);
;         if ((d0 & 3) == 3) SBAR(); }
; }
.LBB0_647:
	v_add_u32_e32 v0, v206, v207
	ds_read_b128 v[66:69], v0 offset:49152
	ds_read_b128 v[70:73], v204
	v_add_u32_e32 v213, v206, v208
	ds_read_b128 v[188:191], v0 offset:57344
	ds_read_b128 v[138:141], v213 offset:49152
	ds_read_b128 v[192:195], v204 offset:1024
	v_add_u32_e32 v214, v206, v209
	v_add_u32_e32 v215, v206, v210
	ds_read_b128 v[246:249], v213 offset:57344
	ds_read_b128 v[250:253], v204 offset:2048
	s_waitcnt lgkmcnt(5)
	v_mfma_f32_32x32x16_bf16 v[82:97], v[66:69], v[70:73], 0
	s_waitcnt lgkmcnt(4)
	v_mfma_f32_32x32x16_bf16 v[66:81], v[188:191], v[70:73], 0
	ds_read_b128 v[188:191], v214 offset:49152
	s_waitcnt lgkmcnt(3)
	v_mfma_f32_32x32x16_bf16 v[82:97], v[138:141], v[192:195], v[82:97]
	ds_read_b128 v[138:141], v214 offset:57344
	s_waitcnt lgkmcnt(3)
	v_mfma_f32_32x32x16_bf16 v[66:81], v[246:249], v[192:195], v[66:81]
	ds_read_b128 v[246:249], v215 offset:49152
	ds_read_b128 v[192:195], v204 offset:3072
	s_waitcnt lgkmcnt(3)
	v_mfma_f32_32x32x16_bf16 v[82:97], v[188:191], v[250:253], v[82:97]
	ds_read_b128 v[188:191], v215 offset:57344
	s_waitcnt lgkmcnt(3)
	v_mfma_f32_32x32x16_bf16 v[66:81], v[138:141], v[250:253], v[66:81]
	ds_read_b128 v[138:141], v0 offset:49280
	ds_read_b128 v[250:253], v204 offset:4096
	s_waitcnt lgkmcnt(3)
	v_mfma_f32_32x32x16_bf16 v[82:97], v[246:249], v[192:195], v[82:97]
	ds_read_b128 v[246:249], v0 offset:57472
	s_waitcnt lgkmcnt(3)
	v_mfma_f32_32x32x16_bf16 v[66:81], v[188:191], v[192:195], v[66:81]
	ds_read_b128 v[188:191], v213 offset:49280
	ds_read_b128 v[192:195], v204 offset:5120
	s_waitcnt lgkmcnt(3)
	v_mfma_f32_32x32x16_bf16 v[82:97], v[138:141], v[250:253], v[82:97]
	ds_read_b128 v[138:141], v213 offset:57472
	s_waitcnt lgkmcnt(3)
	v_mfma_f32_32x32x16_bf16 v[66:81], v[246:249], v[250:253], v[66:81]
	ds_read_b128 v[246:249], v214 offset:49280
	ds_read_b128 v[250:253], v204 offset:6144
	s_waitcnt lgkmcnt(3)
	v_mfma_f32_32x32x16_bf16 v[82:97], v[188:191], v[192:195], v[82:97]
	ds_read_b128 v[188:191], v214 offset:57472
	s_waitcnt lgkmcnt(3)
	v_mfma_f32_32x32x16_bf16 v[66:81], v[138:141], v[192:195], v[66:81]
	ds_read_b128 v[138:141], v215 offset:49280
	ds_read_b128 v[192:195], v204 offset:7168
	s_waitcnt lgkmcnt(3)
	v_mfma_f32_32x32x16_bf16 v[82:97], v[246:249], v[250:253], v[82:97]
	ds_read_b128 v[246:249], v215 offset:57472
	s_waitcnt lgkmcnt(3)
	v_mfma_f32_32x32x16_bf16 v[66:81], v[188:191], v[250:253], v[66:81]
	s_waitcnt lgkmcnt(1)
	v_mfma_f32_32x32x16_bf16 v[82:97], v[138:141], v[192:195], v[82:97]
	s_waitcnt lgkmcnt(0)
	v_mfma_f32_32x32x16_bf16 v[66:81], v[246:249], v[192:195], v[66:81]
	s_mov_b64 s[12:13], -1
	s_and_b64 vcc, exec, s[14:15]
	s_cbranch_vccz .LBB0_651
	s_nop 5
	v_mov_b32_e32 v188, v97
	v_mov_b32_e32 v189, v96
	v_mov_b32_e32 v190, v95
	v_mov_b32_e32 v191, v94
	v_mov_b32_e32 v192, v93
	v_mov_b32_e32 v193, v92
	v_mov_b32_e32 v194, v91
	v_mov_b32_e32 v195, v90
	v_mov_b32_e32 v213, v89
	v_mov_b32_e32 v215, v88
	v_mov_b32_e32 v217, v87
	v_mov_b32_e32 v218, v86
	v_mov_b32_e32 v221, v85
	v_mov_b32_e32 v222, v84
	v_mov_b32_e32 v0, v83
	v_mov_b32_e32 v225, v82
	v_mov_b32_e32 v214, v81
	v_mov_b32_e32 v216, v80
	v_mov_b32_e32 v219, v79
	v_mov_b32_e32 v220, v78
	v_mov_b32_e32 v223, v77
	v_mov_b32_e32 v224, v76
	v_mov_b32_e32 v226, v75
	v_mov_b32_e32 v227, v74
	v_mov_b32_e32 v228, v73
	v_mov_b32_e32 v229, v72
	v_mov_b32_e32 v230, v71
	v_mov_b32_e32 v231, v70
	v_mov_b32_e32 v232, v69
	v_mov_b32_e32 v233, v68
	v_mov_b32_e32 v234, v67
	v_mov_b32_e32 v235, v66
	s_and_saveexec_b64 s[12:13], s[10:11]
	s_cbranch_execz .LBB0_650
	v_mov_b32_e32 v188, 0xff800000
	v_mov_b32_e32 v189, 0xff800000
	v_mov_b32_e32 v190, 0xff800000
	v_mov_b32_e32 v191, 0xff800000
	v_mov_b32_e32 v192, 0xff800000
	v_mov_b32_e32 v193, 0xff800000
	v_mov_b32_e32 v194, 0xff800000
	v_mov_b32_e32 v195, 0xff800000
	v_mov_b32_e32 v213, 0xff800000
	v_mov_b32_e32 v215, 0xff800000
	v_mov_b32_e32 v217, 0xff800000
	v_mov_b32_e32 v218, 0xff800000
	v_mov_b32_e32 v221, 0xff800000
	v_mov_b32_e32 v222, 0xff800000
	v_mov_b32_e32 v0, 0xff800000
	v_mov_b32_e32 v225, 0xff800000
	v_mov_b32_e32 v214, 0xff800000
	v_mov_b32_e32 v216, 0xff800000
	v_mov_b32_e32 v219, 0xff800000
	v_mov_b32_e32 v220, 0xff800000
	v_mov_b32_e32 v223, 0xff800000
	v_mov_b32_e32 v224, 0xff800000
	v_mov_b32_e32 v226, 0xff800000
	v_mov_b32_e32 v227, 0xff800000
	v_mov_b32_e32 v228, 0xff800000
	v_mov_b32_e32 v229, 0xff800000
	v_mov_b32_e32 v230, 0xff800000
	v_mov_b32_e32 v231, 0xff800000
	v_mov_b32_e32 v232, 0xff800000
	v_mov_b32_e32 v233, 0xff800000
	v_mov_b32_e32 v234, 0xff800000
	v_mov_b32_e32 v235, 0xff800000

; #define LAS __attribute__((address_space(3)))
; #define SBAR() __builtin_amdgcn_sched_barrier(0)
; template <int KB>
; __device__ __forceinline__ void qkt(f32x16& p0, f32x16& p1, LAS const unsigned char* K_lds, LAS const unsigned char* q_lds, int r32, int hi) {
;     p0 = f32x16{}; p1 = f32x16{};
;     LAS const unsigned char* kb[4];
; #pragma unroll
;     for (int dd = 0; dd < 4; ++dd) kb[dd] = K_lds + KB * SHM_K + KSWZ(r32, (dd * 16 + hi * 8) * 2);
; #pragma unroll
;     for (int d0 = 0; d0 < 8; ++d0) { LAS const unsigned char* a = kb[d0 & 3] + (d0 >> 2) * 128;
;         const bf16x8 b0 = *(LAS const bf16x8*)(a);
;         const bf16x8 b1 = *(LAS const bf16x8*)(a + 32 * 256);
;         const bf16x8 qv = *(LAS const bf16x8*)(q_lds + d0 * 1024);
;         p0 = __builtin_amdgcn_mfma_f32_32x32x16_bf16(b0, qv, p0, 0, 0, 0);
;         p1 = __builtin_amdgcn_mfma_f32_32x32x16_bf16(b1, qv, p1, 0, 0, 0);
;         if ((d0 & 3) == 3) SBAR(); }
; }
.LBB0_798:
	s_sub_i32 s12, s1, 63
	s_cmp_ge_i32 s12, s83
	s_cbranch_scc1 .LBB0_802
	v_add_u32_e32 v0, v206, v207
	ds_read_b128 v[66:69], v0 offset:32768
	ds_read_b128 v[70:73], v204
	v_add_u32_e32 v143, v206, v208
	ds_read_b128 v[144:147], v0 offset:40960
	ds_read_b128 v[226:229], v143 offset:32768
	ds_read_b128 v[148:151], v204 offset:1024
	v_add_u32_e32 v152, v206, v209
	v_add_u32_e32 v153, v206, v210
	ds_read_b128 v[230:233], v143 offset:40960
	ds_read_b128 v[234:237], v204 offset:2048
	s_waitcnt lgkmcnt(5)
	v_mfma_f32_32x32x16_bf16 v[82:97], v[66:69], v[70:73], 0
	s_waitcnt lgkmcnt(4)
	v_mfma_f32_32x32x16_bf16 v[66:81], v[144:147], v[70:73], 0
	ds_read_b128 v[144:147], v152 offset:32768
	s_waitcnt lgkmcnt(3)
	v_mfma_f32_32x32x16_bf16 v[82:97], v[226:229], v[148:151], v[82:97]
	ds_read_b128 v[226:229], v152 offset:40960
	s_waitcnt lgkmcnt(3)
	v_mfma_f32_32x32x16_bf16 v[66:81], v[230:233], v[148:151], v[66:81]
	ds_read_b128 v[230:233], v153 offset:32768
	ds_read_b128 v[148:151], v204 offset:3072
	s_waitcnt lgkmcnt(3)
	v_mfma_f32_32x32x16_bf16 v[82:97], v[144:147], v[234:237], v[82:97]
	ds_read_b128 v[144:147], v153 offset:40960
	s_waitcnt lgkmcnt(3)
	v_mfma_f32_32x32x16_bf16 v[66:81], v[226:229], v[234:237], v[66:81]
	ds_read_b128 v[226:229], v0 offset:32896
	ds_read_b128 v[234:237], v204 offset:4096
	s_waitcnt lgkmcnt(3)
	v_mfma_f32_32x32x16_bf16 v[82:97], v[230:233], v[148:151], v[82:97]
	ds_read_b128 v[230:233], v0 offset:41088
	s_waitcnt lgkmcnt(3)
	v_mfma_f32_32x32x16_bf16 v[66:81], v[144:147], v[148:151], v[66:81]
	ds_read_b128 v[144:147], v143 offset:32896
	ds_read_b128 v[148:151], v204 offset:5120
	s_waitcnt lgkmcnt(3)
	v_mfma_f32_32x32x16_bf16 v[82:97], v[226:229], v[234:237], v[82:97]
	ds_read_b128 v[226:229], v143 offset:41088
	s_waitcnt lgkmcnt(3)
	v_mfma_f32_32x32x16_bf16 v[66:81], v[230:233], v[234:237], v[66:81]
	ds_read_b128 v[230:233], v152 offset:32896
	ds_read_b128 v[234:237], v204 offset:6144
	s_waitcnt lgkmcnt(3)
	v_mfma_f32_32x32x16_bf16 v[82:97], v[144:147], v[148:151], v[82:97]
	ds_read_b128 v[144:147], v152 offset:41088
	s_waitcnt lgkmcnt(3)
	v_mfma_f32_32x32x16_bf16 v[66:81], v[226:229], v[148:151], v[66:81]
	ds_read_b128 v[226:229], v153 offset:32896
	ds_read_b128 v[148:151], v204 offset:7168
	s_waitcnt lgkmcnt(3)
	v_mfma_f32_32x32x16_bf16 v[82:97], v[230:233], v[234:237], v[82:97]
	ds_read_b128 v[230:233], v153 offset:41088
	s_waitcnt lgkmcnt(3)
	v_mfma_f32_32x32x16_bf16 v[66:81], v[144:147], v[234:237], v[66:81]
	s_waitcnt lgkmcnt(1)
	v_mfma_f32_32x32x16_bf16 v[82:97], v[226:229], v[148:151], v[82:97]
	s_waitcnt lgkmcnt(0)
	v_mfma_f32_32x32x16_bf16 v[66:81], v[230:233], v[148:151], v[66:81]
	s_nop 8
	v_mul_f32_e64 v144, v82, s90
	v_mul_f32_e64 v145, v83, s90
	s_nop 0
	v_pk_mul_f32 v[152:153], v[68:69], s[90:91] op_sel_hi:[1,0]
	v_exp_f32_e64 v0, -|v144|
	v_max_f32_e32 v144, 0, v144
	v_pk_mul_f32 v[160:161], v[70:71], s[90:91] op_sel_hi:[1,0]
	v_pk_mul_f32 v[164:165], v[88:89], s[90:91] op_sel_hi:[1,0]
	v_add_f32_e32 v0, 1.0, v0
	v_log_f32_e32 v146, v0
	v_exp_f32_e64 v0, -|v145|
	v_max_f32_e32 v145, 0, v145
	v_pk_mul_f32 v[168:169], v[74:75], s[90:91] op_sel_hi:[1,0]
	v_pk_mul_f32 v[176:177], v[92:93], s[90:91] op_sel_hi:[1,0]
	v_add_f32_e32 v0, 1.0, v0
	v_log_f32_e32 v147, v0
	v_pk_mul_f32 v[186:187], v[78:79], s[90:91] op_sel_hi:[1,0]
	v_pk_mul_f32 v[222:223], v[96:97], s[90:91] op_sel_hi:[1,0]
	s_cmp_lt_i32 s1, s97
	v_pk_add_f32 v[174:175], v[144:145], v[146:147]
	v_pk_mul_f32 v[146:147], v[66:67], s[90:91] op_sel_hi:[1,0]
	v_pk_add_f32 v[144:145], v[174:175], 0 neg_lo:[1,1] neg_hi:[1,1]
	v_exp_f32_e64 v0, -|v146|
	v_max_f32_e32 v146, 0, v146
	v_pk_fma_f32 v[82:83], v[82:83], s[90:91], v[174:175] op_sel_hi:[1,0,1] neg_lo:[0,0,1] neg_hi:[0,0,1]
	v_pk_mul_f32 v[174:175], v[80:81], s[90:91] op_sel_hi:[1,0]
	v_add_f32_e32 v0, 1.0, v0
	v_log_f32_e32 v148, v0
	v_exp_f32_e64 v0, -|v147|
	v_max_f32_e32 v147, 0, v147
	v_add_f32_e32 v0, 1.0, v0
	v_log_f32_e32 v149, v0
	s_nop 0
	v_pk_add_f32 v[172:173], v[146:147], v[148:149]
	v_pk_mul_f32 v[146:147], v[84:85], s[90:91] op_sel_hi:[1,0]
	v_pk_add_f32 v[150:151], v[172:173], 0 neg_lo:[1,1] neg_hi:[1,1]
	v_exp_f32_e64 v0, -|v146|
	v_max_f32_e32 v146, 0, v146
	v_pk_fma_f32 v[66:67], v[66:67], s[90:91], v[172:173] op_sel_hi:[1,0,1] neg_lo:[0,0,1] neg_hi:[0,0,1]
	v_add_f32_e32 v0, 1.0, v0
	v_log_f32_e32 v148, v0
	v_exp_f32_e64 v0, -|v147|
	v_max_f32_e32 v147, 0, v147
	v_add_f32_e32 v0, 1.0, v0
	v_log_f32_e32 v149, v0
	v_exp_f32_e64 v0, -|v152|
	v_max_f32_e32 v152, 0, v152
	v_pk_add_f32 v[182:183], v[146:147], v[148:149]
	v_add_f32_e32 v0, 1.0, v0
	v_log_f32_e32 v154, v0
	v_exp_f32_e64 v0, -|v153|
	v_max_f32_e32 v153, 0, v153
	v_xor_b32_e32 v147, 0x80000000, v182
	v_pk_fma_f32 v[84:85], v[84:85], s[90:91], v[182:183] op_sel_hi:[1,0,1] neg_lo:[0,0,1] neg_hi:[0,0,1]
	v_add_f32_e32 v0, 1.0, v0
	v_log_f32_e32 v155, v0
	v_xor_b32_e32 v149, 0x80000000, v183
	v_pk_add_f32 v[180:181], v[152:153], v[154:155]
	v_pk_mul_f32 v[152:153], v[86:87], s[90:91] op_sel_hi:[1,0]
	v_xor_b32_e32 v157, 0x80000000, v180
	v_exp_f32_e64 v0, -|v152|
	v_max_f32_e32 v152, 0, v152
	v_xor_b32_e32 v159, 0x80000000, v181
	v_pk_fma_f32 v[68:69], v[68:69], s[90:91], v[180:181] op_sel_hi:[1,0,1] neg_lo:[0,0,1] neg_hi:[0,0,1]
	v_add_f32_e32 v0, 1.0, v0
	v_log_f32_e32 v154, v0
	v_exp_f32_e64 v0, -|v153|
	v_max_f32_e32 v153, 0, v153
	v_add_f32_e32 v0, 1.0, v0
	v_log_f32_e32 v155, v0
	v_exp_f32_e64 v0, -|v160|
	v_max_f32_e32 v160, 0, v160
	v_pk_add_f32 v[190:191], v[152:153], v[154:155]
	v_add_f32_e32 v0, 1.0, v0
	v_log_f32_e32 v162, v0
	v_exp_f32_e64 v0, -|v161|
	v_max_f32_e32 v161, 0, v161
	v_xor_b32_e32 v154, 0x80000000, v190
	v_xor_b32_e32 v152, 0x80000000, v191
	v_add_f32_e32 v0, 1.0, v0
	v_log_f32_e32 v163, v0
	v_exp_f32_e64 v0, -|v164|
	v_max_f32_e32 v164, 0, v164
	v_pk_fma_f32 v[86:87], v[86:87], s[90:91], v[190:191] op_sel_hi:[1,0,1] neg_lo:[0,0,1] neg_hi:[0,0,1]
	v_pk_add_f32 v[184:185], v[160:161], v[162:163]
	v_add_f32_e32 v0, 1.0, v0
	v_log_f32_e32 v166, v0
	v_exp_f32_e64 v0, -|v165|
	v_max_f32_e32 v165, 0, v165
	v_xor_b32_e32 v162, 0x80000000, v184
	v_xor_b32_e32 v160, 0x80000000, v185
	v_add_f32_e32 v0, 1.0, v0
	v_log_f32_e32 v167, v0
	v_pk_fma_f32 v[70:71], v[70:71], s[90:91], v[184:185] op_sel_hi:[1,0,1] neg_lo:[0,0,1] neg_hi:[0,0,1]
	v_pk_add_f32 v[194:195], v[164:165], v[166:167]
	v_pk_mul_f32 v[164:165], v[72:73], s[90:91] op_sel_hi:[1,0]
	v_xor_b32_e32 v153, 0x80000000, v194
	v_exp_f32_e64 v0, -|v164|
	v_max_f32_e32 v164, 0, v164
	v_xor_b32_e32 v155, 0x80000000, v195
	v_pk_fma_f32 v[88:89], v[88:89], s[90:91], v[194:195] op_sel_hi:[1,0,1] neg_lo:[0,0,1] neg_hi:[0,0,1]
	v_add_f32_e32 v0, 1.0, v0
	v_log_f32_e32 v166, v0
	v_exp_f32_e64 v0, -|v165|
	v_max_f32_e32 v165, 0, v165
	v_add_f32_e32 v0, 1.0, v0
	v_log_f32_e32 v167, v0
	s_nop 0
	v_pk_add_f32 v[192:193], v[164:165], v[166:167]
	v_pk_mul_f32 v[164:165], v[90:91], s[90:91] op_sel_hi:[1,0]
	v_xor_b32_e32 v161, 0x80000000, v192
	v_exp_f32_e64 v0, -|v164|
	v_max_f32_e32 v164, 0, v164
	v_xor_b32_e32 v163, 0x80000000, v193
	v_pk_fma_f32 v[72:73], v[72:73], s[90:91], v[192:193] op_sel_hi:[1,0,1] neg_lo:[0,0,1] neg_hi:[0,0,1]
	v_add_f32_e32 v0, 1.0, v0
	v_log_f32_e32 v166, v0
	v_exp_f32_e64 v0, -|v165|
	v_max_f32_e32 v165, 0, v165
	v_add_f32_e32 v0, 1.0, v0
	v_log_f32_e32 v167, v0
	v_exp_f32_e64 v0, -|v168|
	v_max_f32_e32 v168, 0, v168
	v_pk_add_f32 v[198:199], v[164:165], v[166:167]
	v_add_f32_e32 v0, 1.0, v0
	v_log_f32_e32 v170, v0
	v_exp_f32_e64 v0, -|v169|
	v_max_f32_e32 v169, 0, v169
	v_xor_b32_e32 v166, 0x80000000, v198
	v_xor_b32_e32 v164, 0x80000000, v199
	v_add_f32_e32 v0, 1.0, v0
	v_log_f32_e32 v171, v0
	v_exp_f32_e64 v0, -|v176|
	v_max_f32_e32 v176, 0, v176
	v_pk_fma_f32 v[90:91], v[90:91], s[90:91], v[198:199] op_sel_hi:[1,0,1] neg_lo:[0,0,1] neg_hi:[0,0,1]
	v_pk_add_f32 v[196:197], v[168:169], v[170:171]
	v_add_f32_e32 v0, 1.0, v0
	v_log_f32_e32 v178, v0
	v_exp_f32_e64 v0, -|v177|
	v_max_f32_e32 v177, 0, v177
	v_xor_b32_e32 v170, 0x80000000, v196
	v_xor_b32_e32 v168, 0x80000000, v197
	v_add_f32_e32 v0, 1.0, v0
	v_log_f32_e32 v179, v0
	v_pk_fma_f32 v[74:75], v[74:75], s[90:91], v[196:197] op_sel_hi:[1,0,1] neg_lo:[0,0,1] neg_hi:[0,0,1]
	v_pk_add_f32 v[216:217], v[176:177], v[178:179]
	v_pk_mul_f32 v[176:177], v[76:77], s[90:91] op_sel_hi:[1,0]
	v_xor_b32_e32 v165, 0x80000000, v216
	v_exp_f32_e64 v0, -|v176|
	v_max_f32_e32 v176, 0, v176
	v_xor_b32_e32 v167, 0x80000000, v217
	v_pk_fma_f32 v[92:93], v[92:93], s[90:91], v[216:217] op_sel_hi:[1,0,1] neg_lo:[0,0,1] neg_hi:[0,0,1]
	v_add_f32_e32 v0, 1.0, v0
	v_log_f32_e32 v178, v0
	v_exp_f32_e64 v0, -|v177|
	v_max_f32_e32 v177, 0, v177
	v_add_f32_e32 v0, 1.0, v0
	v_log_f32_e32 v179, v0
	s_nop 0
	v_pk_add_f32 v[200:201], v[176:177], v[178:179]
	v_pk_mul_f32 v[176:177], v[94:95], s[90:91] op_sel_hi:[1,0]
	v_xor_b32_e32 v169, 0x80000000, v200
	v_exp_f32_e64 v0, -|v176|
	v_max_f32_e32 v176, 0, v176
	v_xor_b32_e32 v171, 0x80000000, v201
	v_pk_fma_f32 v[76:77], v[76:77], s[90:91], v[200:201] op_sel_hi:[1,0,1] neg_lo:[0,0,1] neg_hi:[0,0,1]
	v_add_f32_e32 v0, 1.0, v0
	v_log_f32_e32 v178, v0
	v_exp_f32_e64 v0, -|v177|
	v_max_f32_e32 v177, 0, v177
	v_add_f32_e32 v0, 1.0, v0
	v_log_f32_e32 v179, v0
	v_exp_f32_e64 v0, -|v186|
	v_max_f32_e32 v186, 0, v186
	v_pk_add_f32 v[218:219], v[176:177], v[178:179]
	v_add_f32_e32 v0, 1.0, v0
	v_log_f32_e32 v188, v0
	v_exp_f32_e64 v0, -|v187|
	v_max_f32_e32 v187, 0, v187
	v_xor_b32_e32 v178, 0x80000000, v218
	v_xor_b32_e32 v176, 0x80000000, v219
	v_add_f32_e32 v0, 1.0, v0
	v_log_f32_e32 v189, v0
	v_exp_f32_e64 v0, -|v222|
	v_max_f32_e32 v222, 0, v222
	v_pk_fma_f32 v[94:95], v[94:95], s[90:91], v[218:219] op_sel_hi:[1,0,1] neg_lo:[0,0,1] neg_hi:[0,0,1]
	v_pk_add_f32 v[220:221], v[186:187], v[188:189]
	v_add_f32_e32 v0, 1.0, v0
	v_log_f32_e32 v224, v0
	v_exp_f32_e64 v0, -|v223|
	v_max_f32_e32 v223, 0, v223
	v_xor_b32_e32 v188, 0x80000000, v220
	v_xor_b32_e32 v186, 0x80000000, v221
	v_add_f32_e32 v0, 1.0, v0
	v_log_f32_e32 v225, v0
	v_exp_f32_e64 v0, -|v174|
	v_max_f32_e32 v174, 0, v174
	v_pk_fma_f32 v[78:79], v[78:79], s[90:91], v[220:221] op_sel_hi:[1,0,1] neg_lo:[0,0,1] neg_hi:[0,0,1]
	v_pk_add_f32 v[222:223], v[222:223], v[224:225]
	v_add_f32_e32 v0, 1.0, v0
	v_log_f32_e32 v182, v0
	v_exp_f32_e64 v0, -|v175|
	v_max_f32_e32 v175, 0, v175
	v_xor_b32_e32 v177, 0x80000000, v222
	v_xor_b32_e32 v179, 0x80000000, v223
	v_add_f32_e32 v0, 1.0, v0
	v_log_f32_e32 v183, v0
	v_pk_fma_f32 v[96:97], v[96:97], s[90:91], v[222:223] op_sel_hi:[1,0,1] neg_lo:[0,0,1] neg_hi:[0,0,1]
	v_pk_add_f32 v[174:175], v[174:175], v[182:183]
	s_nop 0
	v_xor_b32_e32 v187, 0x80000000, v174
	v_xor_b32_e32 v189, 0x80000000, v175
	v_pk_fma_f32 v[80:81], v[80:81], s[90:91], v[174:175] op_sel_hi:[1,0,1] neg_lo:[0,0,1] neg_hi:[0,0,1]
	s_cbranch_scc1 .LBB0_801
	v_cmp_lt_i32_e64 s[72:73], 26, v214
	v_cmp_lt_i32_e64 s[74:75], 27, v214
	v_cmp_lt_i32_e64 s[70:71], 25, v214
	s_or_b64 s[72:73], s[74:75], s[72:73]
	v_cmp_lt_i32_e64 s[68:69], 24, v214
	s_or_b64 s[70:71], s[72:73], s[70:71]
	v_cmp_lt_i32_e64 s[66:67], 19, v214
	s_or_b64 s[68:69], s[70:71], s[68:69]
	v_cmp_lt_i32_e64 s[64:65], 18, v214
	s_or_b64 s[66:67], s[68:69], s[66:67]
	v_cmp_lt_i32_e64 s[62:63], 17, v214
	s_or_b64 s[64:65], s[66:67], s[64:65]
	v_cmp_lt_i32_e64 s[60:61], 16, v214
	s_or_b64 s[62:63], s[64:65], s[62:63]
	v_cmp_lt_i32_e64 s[58:59], 11, v214
	s_or_b64 s[60:61], s[62:63], s[60:61]
	v_cmp_lt_i32_e64 s[56:57], 10, v214
	s_or_b64 s[58:59], s[60:61], s[58:59]
	v_cmp_lt_i32_e64 s[54:55], 9, v214
	s_or_b64 s[56:57], s[58:59], s[56:57]
	v_cmp_lt_i32_e64 s[52:53], 8, v214
	s_or_b64 s[54:55], s[56:57], s[54:55]
	v_cmp_lt_i32_e64 s[50:51], 3, v214
	s_or_b64 s[52:53], s[54:55], s[52:53]
	v_cmp_lt_i32_e64 s[48:49], 2, v214
	s_or_b64 s[50:51], s[52:53], s[50:51]
	v_cmp_lt_i32_e64 s[46:47], 1, v214
	s_or_b64 s[48:49], s[50:51], s[48:49]
	v_cmp_lt_i32_e64 s[44:45], 0, v214
	s_or_b64 s[46:47], s[48:49], s[46:47]
	s_or_b64 s[44:45], s[46:47], s[44:45]
	v_cmp_lt_i32_e64 s[40:41], 58, v214
	v_cndmask_b32_e64 v82, v213, v82, s[44:45]
	v_cndmask_b32_e64 v144, 0, v144, s[44:45]
	v_cmp_lt_i32_e64 s[44:45], 59, v214
	v_cmp_lt_i32_e64 s[38:39], 57, v214
	s_or_b64 s[40:41], s[44:45], s[40:41]
	v_cmp_lt_i32_e64 s[36:37], 56, v214
	s_or_b64 s[38:39], s[40:41], s[38:39]
	v_cmp_lt_i32_e64 s[34:35], 51, v214
	s_or_b64 s[36:37], s[38:39], s[36:37]
	v_cmp_lt_i32_e64 s[30:31], 50, v214
	s_or_b64 s[34:35], s[36:37], s[34:35]
	v_cmp_lt_i32_e64 s[28:29], 49, v214
	s_or_b64 s[30:31], s[34:35], s[30:31]
	v_cmp_lt_i32_e64 s[26:27], 48, v214
	s_or_b64 s[28:29], s[30:31], s[28:29]
	v_cmp_lt_i32_e64 s[24:25], 43, v214
	s_or_b64 s[26:27], s[28:29], s[26:27]
	v_cmp_lt_i32_e64 s[22:23], 42, v214
	s_or_b64 s[24:25], s[26:27], s[24:25]
	v_cmp_lt_i32_e64 s[20:21], 41, v214
	s_or_b64 s[22:23], s[24:25], s[22:23]
	v_cmp_lt_i32_e64 s[18:19], 40, v214
	s_or_b64 s[20:21], s[22:23], s[20:21]
	v_cmp_lt_i32_e64 s[16:17], 35, v214
	s_or_b64 s[18:19], s[20:21], s[18:19]
	v_cmp_lt_i32_e64 s[14:15], 34, v214
	s_or_b64 s[16:17], s[18:19], s[16:17]
	v_cmp_lt_i32_e64 s[12:13], 33, v214
	s_or_b64 s[14:15], s[16:17], s[14:15]
	v_cmp_lt_i32_e32 vcc, 32, v214
	s_or_b64 s[12:13], s[14:15], s[12:13]
	s_or_b64 vcc, s[12:13], vcc
	v_cndmask_b32_e64 v97, v213, v97, s[74:75]
	v_cndmask_b32_e64 v96, v213, v96, s[72:73]
	v_cndmask_b32_e64 v95, v213, v95, s[70:71]
	v_cndmask_b32_e64 v94, v213, v94, s[68:69]
	v_cndmask_b32_e64 v93, v213, v93, s[66:67]
	v_cndmask_b32_e64 v92, v213, v92, s[64:65]
	v_cndmask_b32_e64 v91, v213, v91, s[62:63]
	v_cndmask_b32_e64 v90, v213, v90, s[60:61]
	v_cndmask_b32_e64 v89, v213, v89, s[58:59]
	v_cndmask_b32_e64 v88, v213, v88, s[56:57]
	v_cndmask_b32_e64 v87, v213, v87, s[54:55]
	v_cndmask_b32_e64 v86, v213, v86, s[52:53]
	v_cndmask_b32_e64 v85, v213, v85, s[50:51]
	v_cndmask_b32_e64 v84, v213, v84, s[48:49]
	v_cndmask_b32_e64 v83, v213, v83, s[46:47]
	v_cndmask_b32_e64 v145, 0, v145, s[46:47]
	v_cndmask_b32_e64 v147, 0, v147, s[48:49]
	v_cndmask_b32_e64 v149, 0, v149, s[50:51]
	v_cndmask_b32_e64 v154, 0, v154, s[52:53]
	v_cndmask_b32_e64 v152, 0, v152, s[54:55]
	v_cndmask_b32_e64 v153, 0, v153, s[56:57]
	v_cndmask_b32_e64 v155, 0, v155, s[58:59]
	v_cndmask_b32_e64 v166, 0, v166, s[60:61]
	v_cndmask_b32_e64 v164, 0, v164, s[62:63]
	v_cndmask_b32_e64 v165, 0, v165, s[64:65]
	v_cndmask_b32_e64 v167, 0, v167, s[66:67]
	v_cndmask_b32_e64 v178, 0, v178, s[68:69]
	v_cndmask_b32_e64 v176, 0, v176, s[70:71]
	v_cndmask_b32_e64 v177, 0, v177, s[72:73]
	v_cndmask_b32_e64 v179, 0, v179, s[74:75]
	v_cndmask_b32_e64 v81, v213, v81, s[44:45]
	v_cndmask_b32_e64 v80, v213, v80, s[40:41]
	v_cndmask_b32_e64 v79, v213, v79, s[38:39]
	v_cndmask_b32_e64 v78, v213, v78, s[36:37]
	v_cndmask_b32_e64 v77, v213, v77, s[34:35]
	v_cndmask_b32_e64 v76, v213, v76, s[30:31]
	v_cndmask_b32_e64 v75, v213, v75, s[28:29]
	v_cndmask_b32_e64 v74, v213, v74, s[26:27]
	v_cndmask_b32_e64 v73, v213, v73, s[24:25]
	v_cndmask_b32_e64 v72, v213, v72, s[22:23]
	v_cndmask_b32_e64 v71, v213, v71, s[20:21]
	v_cndmask_b32_e64 v70, v213, v70, s[18:19]
	v_cndmask_b32_e64 v69, v213, v69, s[16:17]
	v_cndmask_b32_e64 v68, v213, v68, s[14:15]
	v_cndmask_b32_e64 v67, v213, v67, s[12:13]
	v_cndmask_b32_e32 v66, v213, v66, vcc
	v_cndmask_b32_e32 v150, 0, v150, vcc
	v_cndmask_b32_e64 v151, 0, v151, s[12:13]
	v_cndmask_b32_e64 v157, 0, v157, s[14:15]
	v_cndmask_b32_e64 v159, 0, v159, s[16:17]
	v_cndmask_b32_e64 v162, 0, v162, s[18:19]
	v_cndmask_b32_e64 v160, 0, v160, s[20:21]
	v_cndmask_b32_e64 v161, 0, v161, s[22:23]
	v_cndmask_b32_e64 v163, 0, v163, s[24:25]
	v_cndmask_b32_e64 v170, 0, v170, s[26:27]
	v_cndmask_b32_e64 v168, 0, v168, s[28:29]
	v_cndmask_b32_e64 v169, 0, v169, s[30:31]
	v_cndmask_b32_e64 v171, 0, v171, s[34:35]
	v_cndmask_b32_e64 v188, 0, v188, s[36:37]
	v_cndmask_b32_e64 v186, 0, v186, s[38:39]
	v_cndmask_b32_e64 v187, 0, v187, s[40:41]
	v_cndmask_b32_e64 v189, 0, v189, s[44:45]

; #define LAS __attribute__((address_space(3)))
; #define SBAR() __builtin_amdgcn_sched_barrier(0)
; template <int KB>
; __device__ __forceinline__ void qkt(f32x16& p0, f32x16& p1, LAS const unsigned char* K_lds, LAS const unsigned char* q_lds, int r32, int hi) {
;     p0 = f32x16{}; p1 = f32x16{};
;     LAS const unsigned char* kb[4];
; #pragma unroll
;     for (int dd = 0; dd < 4; ++dd) kb[dd] = K_lds + KB * SHM_K + KSWZ(r32, (dd * 16 + hi * 8) * 2);
; #pragma unroll
;     for (int d0 = 0; d0 < 8; ++d0) { LAS const unsigned char* a = kb[d0 & 3] + (d0 >> 2) * 128;
;         const bf16x8 b0 = *(LAS const bf16x8*)(a);
;         const bf16x8 b1 = *(LAS const bf16x8*)(a + 32 * 256);
;         const bf16x8 qv = *(LAS const bf16x8*)(q_lds + d0 * 1024);
;         p0 = __builtin_amdgcn_mfma_f32_32x32x16_bf16(b0, qv, p0, 0, 0, 0);
;         p1 = __builtin_amdgcn_mfma_f32_32x32x16_bf16(b1, qv, p1, 0, 0, 0);
;         if ((d0 & 3) == 3) SBAR(); }
; }
.LBB0_806:
	s_add_i32 s12, s1, 0xffffff81
	s_cmp_ge_i32 s12, s83
	s_cbranch_scc1 .LBB0_810
	v_add_u32_e32 v0, v206, v207
	ds_read_b128 v[66:69], v0 offset:49152
	ds_read_b128 v[70:73], v204
	v_add_u32_e32 v143, v206, v208
	ds_read_b128 v[144:147], v0 offset:57344
	ds_read_b128 v[226:229], v143 offset:49152
	ds_read_b128 v[148:151], v204 offset:1024
	v_add_u32_e32 v152, v206, v209
	v_add_u32_e32 v153, v206, v210
	ds_read_b128 v[230:233], v143 offset:57344
	ds_read_b128 v[234:237], v204 offset:2048
	s_waitcnt lgkmcnt(5)
	v_mfma_f32_32x32x16_bf16 v[82:97], v[66:69], v[70:73], 0
	s_waitcnt lgkmcnt(4)
	v_mfma_f32_32x32x16_bf16 v[66:81], v[144:147], v[70:73], 0
	ds_read_b128 v[144:147], v152 offset:49152
	s_waitcnt lgkmcnt(3)
	v_mfma_f32_32x32x16_bf16 v[82:97], v[226:229], v[148:151], v[82:97]
	ds_read_b128 v[226:229], v152 offset:57344
	s_waitcnt lgkmcnt(3)
	v_mfma_f32_32x32x16_bf16 v[66:81], v[230:233], v[148:151], v[66:81]
	ds_read_b128 v[230:233], v153 offset:49152
	ds_read_b128 v[148:151], v204 offset:3072
	s_waitcnt lgkmcnt(3)
	v_mfma_f32_32x32x16_bf16 v[82:97], v[144:147], v[234:237], v[82:97]
	ds_read_b128 v[144:147], v153 offset:57344
	s_waitcnt lgkmcnt(3)
	v_mfma_f32_32x32x16_bf16 v[66:81], v[226:229], v[234:237], v[66:81]
	ds_read_b128 v[226:229], v0 offset:49280
	ds_read_b128 v[234:237], v204 offset:4096
	s_waitcnt lgkmcnt(3)
	v_mfma_f32_32x32x16_bf16 v[82:97], v[230:233], v[148:151], v[82:97]
	ds_read_b128 v[230:233], v0 offset:57472
	s_waitcnt lgkmcnt(3)
	v_mfma_f32_32x32x16_bf16 v[66:81], v[144:147], v[148:151], v[66:81]
	ds_read_b128 v[144:147], v143 offset:49280
	ds_read_b128 v[148:151], v204 offset:5120
	s_waitcnt lgkmcnt(3)
	v_mfma_f32_32x32x16_bf16 v[82:97], v[226:229], v[234:237], v[82:97]
	ds_read_b128 v[226:229], v143 offset:57472
	s_waitcnt lgkmcnt(3)
	v_mfma_f32_32x32x16_bf16 v[66:81], v[230:233], v[234:237], v[66:81]
	ds_read_b128 v[230:233], v152 offset:49280
	ds_read_b128 v[234:237], v204 offset:6144
	s_waitcnt lgkmcnt(3)
	v_mfma_f32_32x32x16_bf16 v[82:97], v[144:147], v[148:151], v[82:97]
	ds_read_b128 v[144:147], v152 offset:57472
	s_waitcnt lgkmcnt(3)
	v_mfma_f32_32x32x16_bf16 v[66:81], v[226:229], v[148:151], v[66:81]
	ds_read_b128 v[226:229], v153 offset:49280
	ds_read_b128 v[148:151], v204 offset:7168
	s_waitcnt lgkmcnt(3)
	v_mfma_f32_32x32x16_bf16 v[82:97], v[230:233], v[234:237], v[82:97]
	ds_read_b128 v[230:233], v153 offset:57472
	s_waitcnt lgkmcnt(3)
	v_mfma_f32_32x32x16_bf16 v[66:81], v[144:147], v[234:237], v[66:81]
	s_waitcnt lgkmcnt(1)
	v_mfma_f32_32x32x16_bf16 v[82:97], v[226:229], v[148:151], v[82:97]
	s_waitcnt lgkmcnt(0)
	v_mfma_f32_32x32x16_bf16 v[66:81], v[230:233], v[148:151], v[66:81]
	s_nop 8
	v_mul_f32_e64 v144, v82, s90
	v_mul_f32_e64 v145, v83, s90
	s_nop 0
	v_pk_mul_f32 v[152:153], v[68:69], s[90:91] op_sel_hi:[1,0]
	v_exp_f32_e64 v0, -|v144|
	v_max_f32_e32 v144, 0, v144
	v_pk_mul_f32 v[160:161], v[70:71], s[90:91] op_sel_hi:[1,0]
	v_pk_mul_f32 v[164:165], v[88:89], s[90:91] op_sel_hi:[1,0]
	v_add_f32_e32 v0, 1.0, v0
	v_log_f32_e32 v146, v0
	v_exp_f32_e64 v0, -|v145|
	v_max_f32_e32 v145, 0, v145
	v_pk_mul_f32 v[168:169], v[74:75], s[90:91] op_sel_hi:[1,0]
	v_pk_mul_f32 v[176:177], v[92:93], s[90:91] op_sel_hi:[1,0]
	v_add_f32_e32 v0, 1.0, v0
	v_log_f32_e32 v147, v0
	v_pk_mul_f32 v[186:187], v[78:79], s[90:91] op_sel_hi:[1,0]
	v_pk_mul_f32 v[222:223], v[96:97], s[90:91] op_sel_hi:[1,0]
	s_sub_i32 s12, s1, 64
	v_pk_add_f32 v[174:175], v[144:145], v[146:147]
	v_pk_mul_f32 v[146:147], v[66:67], s[90:91] op_sel_hi:[1,0]
	v_pk_add_f32 v[144:145], v[174:175], 0 neg_lo:[1,1] neg_hi:[1,1]
	v_exp_f32_e64 v0, -|v146|
	v_max_f32_e32 v146, 0, v146
	v_pk_fma_f32 v[82:83], v[82:83], s[90:91], v[174:175] op_sel_hi:[1,0,1] neg_lo:[0,0,1] neg_hi:[0,0,1]
	v_pk_mul_f32 v[174:175], v[80:81], s[90:91] op_sel_hi:[1,0]
	v_add_f32_e32 v0, 1.0, v0
	v_log_f32_e32 v148, v0
	v_exp_f32_e64 v0, -|v147|
	v_max_f32_e32 v147, 0, v147
	s_cmp_lt_i32 s12, s97
	v_add_f32_e32 v0, 1.0, v0
	v_log_f32_e32 v149, v0
	s_nop 0
	v_pk_add_f32 v[172:173], v[146:147], v[148:149]
	v_pk_mul_f32 v[146:147], v[84:85], s[90:91] op_sel_hi:[1,0]
	v_pk_add_f32 v[150:151], v[172:173], 0 neg_lo:[1,1] neg_hi:[1,1]
	v_exp_f32_e64 v0, -|v146|
	v_max_f32_e32 v146, 0, v146
	v_pk_fma_f32 v[66:67], v[66:67], s[90:91], v[172:173] op_sel_hi:[1,0,1] neg_lo:[0,0,1] neg_hi:[0,0,1]
	v_add_f32_e32 v0, 1.0, v0
	v_log_f32_e32 v148, v0
	v_exp_f32_e64 v0, -|v147|
	v_max_f32_e32 v147, 0, v147
	v_add_f32_e32 v0, 1.0, v0
	v_log_f32_e32 v149, v0
	v_exp_f32_e64 v0, -|v152|
	v_max_f32_e32 v152, 0, v152
	v_pk_add_f32 v[182:183], v[146:147], v[148:149]
	v_add_f32_e32 v0, 1.0, v0
	v_log_f32_e32 v154, v0
	v_exp_f32_e64 v0, -|v153|
	v_max_f32_e32 v153, 0, v153
	v_xor_b32_e32 v147, 0x80000000, v182
	v_pk_fma_f32 v[84:85], v[84:85], s[90:91], v[182:183] op_sel_hi:[1,0,1] neg_lo:[0,0,1] neg_hi:[0,0,1]
	v_add_f32_e32 v0, 1.0, v0
	v_log_f32_e32 v155, v0
	v_xor_b32_e32 v149, 0x80000000, v183
	v_pk_add_f32 v[180:181], v[152:153], v[154:155]
	v_pk_mul_f32 v[152:153], v[86:87], s[90:91] op_sel_hi:[1,0]
	v_xor_b32_e32 v157, 0x80000000, v180
	v_exp_f32_e64 v0, -|v152|
	v_max_f32_e32 v152, 0, v152
	v_xor_b32_e32 v159, 0x80000000, v181
	v_pk_fma_f32 v[68:69], v[68:69], s[90:91], v[180:181] op_sel_hi:[1,0,1] neg_lo:[0,0,1] neg_hi:[0,0,1]
	v_add_f32_e32 v0, 1.0, v0
	v_log_f32_e32 v154, v0
	v_exp_f32_e64 v0, -|v153|
	v_max_f32_e32 v153, 0, v153
	v_add_f32_e32 v0, 1.0, v0
	v_log_f32_e32 v155, v0
	v_exp_f32_e64 v0, -|v160|
	v_max_f32_e32 v160, 0, v160
	v_pk_add_f32 v[190:191], v[152:153], v[154:155]
	v_add_f32_e32 v0, 1.0, v0
	v_log_f32_e32 v162, v0
	v_exp_f32_e64 v0, -|v161|
	v_max_f32_e32 v161, 0, v161
	v_xor_b32_e32 v154, 0x80000000, v190
	v_xor_b32_e32 v152, 0x80000000, v191
	v_add_f32_e32 v0, 1.0, v0
	v_log_f32_e32 v163, v0
	v_exp_f32_e64 v0, -|v164|
	v_max_f32_e32 v164, 0, v164
	v_pk_fma_f32 v[86:87], v[86:87], s[90:91], v[190:191] op_sel_hi:[1,0,1] neg_lo:[0,0,1] neg_hi:[0,0,1]
	v_pk_add_f32 v[184:185], v[160:161], v[162:163]
	v_add_f32_e32 v0, 1.0, v0
	v_log_f32_e32 v166, v0
	v_exp_f32_e64 v0, -|v165|
	v_max_f32_e32 v165, 0, v165
	v_xor_b32_e32 v162, 0x80000000, v184
	v_xor_b32_e32 v160, 0x80000000, v185
	v_add_f32_e32 v0, 1.0, v0
	v_log_f32_e32 v167, v0
	v_pk_fma_f32 v[70:71], v[70:71], s[90:91], v[184:185] op_sel_hi:[1,0,1] neg_lo:[0,0,1] neg_hi:[0,0,1]
	v_pk_add_f32 v[194:195], v[164:165], v[166:167]
	v_pk_mul_f32 v[164:165], v[72:73], s[90:91] op_sel_hi:[1,0]
	v_xor_b32_e32 v153, 0x80000000, v194
	v_exp_f32_e64 v0, -|v164|
	v_max_f32_e32 v164, 0, v164
	v_xor_b32_e32 v155, 0x80000000, v195
	v_pk_fma_f32 v[88:89], v[88:89], s[90:91], v[194:195] op_sel_hi:[1,0,1] neg_lo:[0,0,1] neg_hi:[0,0,1]
	v_add_f32_e32 v0, 1.0, v0
	v_log_f32_e32 v166, v0
	v_exp_f32_e64 v0, -|v165|
	v_max_f32_e32 v165, 0, v165
	v_add_f32_e32 v0, 1.0, v0
	v_log_f32_e32 v167, v0
	s_nop 0
	v_pk_add_f32 v[192:193], v[164:165], v[166:167]
	v_pk_mul_f32 v[164:165], v[90:91], s[90:91] op_sel_hi:[1,0]
	v_xor_b32_e32 v161, 0x80000000, v192
	v_exp_f32_e64 v0, -|v164|
	v_max_f32_e32 v164, 0, v164
	v_xor_b32_e32 v163, 0x80000000, v193
	v_pk_fma_f32 v[72:73], v[72:73], s[90:91], v[192:193] op_sel_hi:[1,0,1] neg_lo:[0,0,1] neg_hi:[0,0,1]
	v_add_f32_e32 v0, 1.0, v0
	v_log_f32_e32 v166, v0
	v_exp_f32_e64 v0, -|v165|
	v_max_f32_e32 v165, 0, v165
	v_add_f32_e32 v0, 1.0, v0
	v_log_f32_e32 v167, v0
	v_exp_f32_e64 v0, -|v168|
	v_max_f32_e32 v168, 0, v168
	v_pk_add_f32 v[198:199], v[164:165], v[166:167]
	v_add_f32_e32 v0, 1.0, v0
	v_log_f32_e32 v170, v0
	v_exp_f32_e64 v0, -|v169|
	v_max_f32_e32 v169, 0, v169
	v_xor_b32_e32 v166, 0x80000000, v198
	v_xor_b32_e32 v164, 0x80000000, v199
	v_add_f32_e32 v0, 1.0, v0
	v_log_f32_e32 v171, v0
	v_exp_f32_e64 v0, -|v176|
	v_max_f32_e32 v176, 0, v176
	v_pk_fma_f32 v[90:91], v[90:91], s[90:91], v[198:199] op_sel_hi:[1,0,1] neg_lo:[0,0,1] neg_hi:[0,0,1]
	v_pk_add_f32 v[196:197], v[168:169], v[170:171]
	v_add_f32_e32 v0, 1.0, v0
	v_log_f32_e32 v178, v0
	v_exp_f32_e64 v0, -|v177|
	v_max_f32_e32 v177, 0, v177
	v_xor_b32_e32 v170, 0x80000000, v196
	v_xor_b32_e32 v168, 0x80000000, v197
	v_add_f32_e32 v0, 1.0, v0
	v_log_f32_e32 v179, v0
	v_pk_fma_f32 v[74:75], v[74:75], s[90:91], v[196:197] op_sel_hi:[1,0,1] neg_lo:[0,0,1] neg_hi:[0,0,1]
	v_pk_add_f32 v[216:217], v[176:177], v[178:179]
	v_pk_mul_f32 v[176:177], v[76:77], s[90:91] op_sel_hi:[1,0]
	v_xor_b32_e32 v165, 0x80000000, v216
	v_exp_f32_e64 v0, -|v176|
	v_max_f32_e32 v176, 0, v176
	v_xor_b32_e32 v167, 0x80000000, v217
	v_pk_fma_f32 v[92:93], v[92:93], s[90:91], v[216:217] op_sel_hi:[1,0,1] neg_lo:[0,0,1] neg_hi:[0,0,1]
	v_add_f32_e32 v0, 1.0, v0
	v_log_f32_e32 v178, v0
	v_exp_f32_e64 v0, -|v177|
	v_max_f32_e32 v177, 0, v177
	v_add_f32_e32 v0, 1.0, v0
	v_log_f32_e32 v179, v0
	s_nop 0
	v_pk_add_f32 v[200:201], v[176:177], v[178:179]
	v_pk_mul_f32 v[176:177], v[94:95], s[90:91] op_sel_hi:[1,0]
	v_xor_b32_e32 v169, 0x80000000, v200
	v_exp_f32_e64 v0, -|v176|
	v_max_f32_e32 v176, 0, v176
	v_xor_b32_e32 v171, 0x80000000, v201
	v_pk_fma_f32 v[76:77], v[76:77], s[90:91], v[200:201] op_sel_hi:[1,0,1] neg_lo:[0,0,1] neg_hi:[0,0,1]
	v_add_f32_e32 v0, 1.0, v0
	v_log_f32_e32 v178, v0
	v_exp_f32_e64 v0, -|v177|
	v_max_f32_e32 v177, 0, v177
	v_add_f32_e32 v0, 1.0, v0
	v_log_f32_e32 v179, v0
	v_exp_f32_e64 v0, -|v186|
	v_max_f32_e32 v186, 0, v186
	v_pk_add_f32 v[218:219], v[176:177], v[178:179]
	v_add_f32_e32 v0, 1.0, v0
	v_log_f32_e32 v188, v0
	v_exp_f32_e64 v0, -|v187|
	v_max_f32_e32 v187, 0, v187
	v_xor_b32_e32 v178, 0x80000000, v218
	v_xor_b32_e32 v176, 0x80000000, v219
	v_add_f32_e32 v0, 1.0, v0
	v_log_f32_e32 v189, v0
	v_exp_f32_e64 v0, -|v222|
	v_max_f32_e32 v222, 0, v222
	v_pk_fma_f32 v[94:95], v[94:95], s[90:91], v[218:219] op_sel_hi:[1,0,1] neg_lo:[0,0,1] neg_hi:[0,0,1]
	v_pk_add_f32 v[220:221], v[186:187], v[188:189]
	v_add_f32_e32 v0, 1.0, v0
	v_log_f32_e32 v224, v0
	v_exp_f32_e64 v0, -|v223|
	v_max_f32_e32 v223, 0, v223
	v_xor_b32_e32 v188, 0x80000000, v220
	v_xor_b32_e32 v186, 0x80000000, v221
	v_add_f32_e32 v0, 1.0, v0
	v_log_f32_e32 v225, v0
	v_exp_f32_e64 v0, -|v174|
	v_max_f32_e32 v174, 0, v174
	v_pk_fma_f32 v[78:79], v[78:79], s[90:91], v[220:221] op_sel_hi:[1,0,1] neg_lo:[0,0,1] neg_hi:[0,0,1]
	v_pk_add_f32 v[222:223], v[222:223], v[224:225]
	v_add_f32_e32 v0, 1.0, v0
	v_log_f32_e32 v182, v0
	v_exp_f32_e64 v0, -|v175|
	v_max_f32_e32 v175, 0, v175
	v_xor_b32_e32 v177, 0x80000000, v222
	v_xor_b32_e32 v179, 0x80000000, v223
	v_add_f32_e32 v0, 1.0, v0
	v_log_f32_e32 v183, v0
	v_pk_fma_f32 v[96:97], v[96:97], s[90:91], v[222:223] op_sel_hi:[1,0,1] neg_lo:[0,0,1] neg_hi:[0,0,1]
	v_pk_add_f32 v[174:175], v[174:175], v[182:183]
	s_nop 0
	v_xor_b32_e32 v187, 0x80000000, v174
	v_xor_b32_e32 v189, 0x80000000, v175
	v_pk_fma_f32 v[80:81], v[80:81], s[90:91], v[174:175] op_sel_hi:[1,0,1] neg_lo:[0,0,1] neg_hi:[0,0,1]
	s_cbranch_scc1 .LBB0_809
	v_add_u32_e32 v0, 64, v214
	v_cmp_lt_i32_e64 s[72:73], 26, v0
	v_cmp_lt_i32_e64 s[74:75], 27, v0
	v_cmp_lt_i32_e64 s[70:71], 25, v0
	s_or_b64 s[72:73], s[74:75], s[72:73]
	v_cmp_lt_i32_e64 s[68:69], 24, v0
	s_or_b64 s[70:71], s[72:73], s[70:71]
	v_cmp_lt_i32_e64 s[66:67], 19, v0
	s_or_b64 s[68:69], s[70:71], s[68:69]
	v_cmp_lt_i32_e64 s[64:65], 18, v0
	s_or_b64 s[66:67], s[68:69], s[66:67]
	v_cmp_lt_i32_e64 s[62:63], 17, v0
	s_or_b64 s[64:65], s[66:67], s[64:65]
	v_cmp_lt_i32_e64 s[60:61], 16, v0
	s_or_b64 s[62:63], s[64:65], s[62:63]
	v_cmp_lt_i32_e64 s[58:59], 11, v0
	s_or_b64 s[60:61], s[62:63], s[60:61]
	v_cmp_lt_i32_e64 s[56:57], 10, v0
	s_or_b64 s[58:59], s[60:61], s[58:59]
	v_cmp_lt_i32_e64 s[54:55], 9, v0
	s_or_b64 s[56:57], s[58:59], s[56:57]
	v_cmp_lt_i32_e64 s[52:53], 8, v0
	s_or_b64 s[54:55], s[56:57], s[54:55]
	v_cmp_lt_i32_e64 s[50:51], 3, v0
	s_or_b64 s[52:53], s[54:55], s[52:53]
	v_cmp_lt_i32_e64 s[48:49], 2, v0
	s_or_b64 s[50:51], s[52:53], s[50:51]
	v_cmp_lt_i32_e64 s[46:47], 1, v0
	s_or_b64 s[48:49], s[50:51], s[48:49]
	v_cmp_lt_i32_e64 s[44:45], 0, v0
	s_or_b64 s[46:47], s[48:49], s[46:47]
	s_or_b64 s[44:45], s[46:47], s[44:45]
	v_cmp_lt_i32_e64 s[40:41], 58, v0
	v_cndmask_b32_e64 v82, v213, v82, s[44:45]
	v_cndmask_b32_e64 v144, 0, v144, s[44:45]
	v_cmp_lt_i32_e64 s[44:45], 59, v0
	v_cmp_lt_i32_e64 s[38:39], 57, v0
	s_or_b64 s[40:41], s[44:45], s[40:41]
	v_cmp_lt_i32_e64 s[36:37], 56, v0
	s_or_b64 s[38:39], s[40:41], s[38:39]
	v_cmp_lt_i32_e64 s[34:35], 51, v0
	s_or_b64 s[36:37], s[38:39], s[36:37]
	v_cmp_lt_i32_e64 s[30:31], 50, v0
	s_or_b64 s[34:35], s[36:37], s[34:35]
	v_cmp_lt_i32_e64 s[28:29], 49, v0
	s_or_b64 s[30:31], s[34:35], s[30:31]
	v_cmp_lt_i32_e64 s[26:27], 48, v0
	s_or_b64 s[28:29], s[30:31], s[28:29]
	v_cmp_lt_i32_e64 s[24:25], 43, v0
	s_or_b64 s[26:27], s[28:29], s[26:27]
	v_cmp_lt_i32_e64 s[22:23], 42, v0
	s_or_b64 s[24:25], s[26:27], s[24:25]
	v_cmp_lt_i32_e64 s[20:21], 41, v0
	s_or_b64 s[22:23], s[24:25], s[22:23]
	v_cmp_lt_i32_e64 s[18:19], 40, v0
	s_or_b64 s[20:21], s[22:23], s[20:21]
	v_cmp_lt_i32_e64 s[16:17], 35, v0
	s_or_b64 s[18:19], s[20:21], s[18:19]
	v_cmp_lt_i32_e64 s[14:15], 34, v0
	s_or_b64 s[16:17], s[18:19], s[16:17]
	v_cmp_lt_i32_e64 s[12:13], 33, v0
	s_or_b64 s[14:15], s[16:17], s[14:15]
	v_cmp_lt_i32_e32 vcc, 32, v0
	s_or_b64 s[12:13], s[14:15], s[12:13]
	s_or_b64 vcc, s[12:13], vcc
	v_cndmask_b32_e64 v97, v213, v97, s[74:75]
	v_cndmask_b32_e64 v96, v213, v96, s[72:73]
	v_cndmask_b32_e64 v95, v213, v95, s[70:71]
	v_cndmask_b32_e64 v94, v213, v94, s[68:69]
	v_cndmask_b32_e64 v93, v213, v93, s[66:67]
	v_cndmask_b32_e64 v92, v213, v92, s[64:65]
	v_cndmask_b32_e64 v91, v213, v91, s[62:63]
	v_cndmask_b32_e64 v90, v213, v90, s[60:61]
	v_cndmask_b32_e64 v89, v213, v89, s[58:59]
	v_cndmask_b32_e64 v88, v213, v88, s[56:57]
	v_cndmask_b32_e64 v87, v213, v87, s[54:55]
	v_cndmask_b32_e64 v86, v213, v86, s[52:53]
	v_cndmask_b32_e64 v85, v213, v85, s[50:51]
	v_cndmask_b32_e64 v84, v213, v84, s[48:49]
	v_cndmask_b32_e64 v83, v213, v83, s[46:47]
	v_cndmask_b32_e64 v145, 0, v145, s[46:47]
	v_cndmask_b32_e64 v147, 0, v147, s[48:49]
	v_cndmask_b32_e64 v149, 0, v149, s[50:51]
	v_cndmask_b32_e64 v154, 0, v154, s[52:53]
	v_cndmask_b32_e64 v152, 0, v152, s[54:55]
	v_cndmask_b32_e64 v153, 0, v153, s[56:57]
	v_cndmask_b32_e64 v155, 0, v155, s[58:59]
	v_cndmask_b32_e64 v166, 0, v166, s[60:61]
	v_cndmask_b32_e64 v164, 0, v164, s[62:63]
	v_cndmask_b32_e64 v165, 0, v165, s[64:65]
	v_cndmask_b32_e64 v167, 0, v167, s[66:67]
	v_cndmask_b32_e64 v178, 0, v178, s[68:69]
	v_cndmask_b32_e64 v176, 0, v176, s[70:71]
	v_cndmask_b32_e64 v177, 0, v177, s[72:73]
	v_cndmask_b32_e64 v179, 0, v179, s[74:75]
	v_cndmask_b32_e64 v81, v213, v81, s[44:45]
	v_cndmask_b32_e64 v80, v213, v80, s[40:41]
	v_cndmask_b32_e64 v79, v213, v79, s[38:39]
	v_cndmask_b32_e64 v78, v213, v78, s[36:37]
	v_cndmask_b32_e64 v77, v213, v77, s[34:35]
	v_cndmask_b32_e64 v76, v213, v76, s[30:31]
	v_cndmask_b32_e64 v75, v213, v75, s[28:29]
	v_cndmask_b32_e64 v74, v213, v74, s[26:27]
	v_cndmask_b32_e64 v73, v213, v73, s[24:25]
	v_cndmask_b32_e64 v72, v213, v72, s[22:23]
	v_cndmask_b32_e64 v71, v213, v71, s[20:21]
	v_cndmask_b32_e64 v70, v213, v70, s[18:19]
	v_cndmask_b32_e64 v69, v213, v69, s[16:17]
	v_cndmask_b32_e64 v68, v213, v68, s[14:15]
	v_cndmask_b32_e64 v67, v213, v67, s[12:13]
	v_cndmask_b32_e32 v66, v213, v66, vcc
	v_cndmask_b32_e32 v150, 0, v150, vcc
	v_cndmask_b32_e64 v151, 0, v151, s[12:13]
	v_cndmask_b32_e64 v157, 0, v157, s[14:15]
	v_cndmask_b32_e64 v159, 0, v159, s[16:17]
	v_cndmask_b32_e64 v162, 0, v162, s[18:19]
	v_cndmask_b32_e64 v160, 0, v160, s[20:21]
	v_cndmask_b32_e64 v161, 0, v161, s[22:23]
	v_cndmask_b32_e64 v163, 0, v163, s[24:25]
	v_cndmask_b32_e64 v170, 0, v170, s[26:27]
	v_cndmask_b32_e64 v168, 0, v168, s[28:29]
	v_cndmask_b32_e64 v169, 0, v169, s[30:31]
	v_cndmask_b32_e64 v171, 0, v171, s[34:35]
	v_cndmask_b32_e64 v188, 0, v188, s[36:37]
	v_cndmask_b32_e64 v186, 0, v186, s[38:39]
	v_cndmask_b32_e64 v187, 0, v187, s[40:41]
	v_cndmask_b32_e64 v189, 0, v189, s[44:45]
